# speedup vs baseline: 1.0526x; 1.0091x over previous
.LBB3_81:
	s_mov_b64 s[8:9], 0x180
	s_add_u32 s72, s66, 0x180
	s_addc_u32 s73, s67, 0
	s_add_u32 s74, s68, 0x180
	s_addc_u32 s75, s69, 0
	s_barrier
	v_readfirstlane_b32 s12, v109
	s_and_b64 vcc, exec, s[2:3]
	s_cbranch_vccnz .LBB3_83
	v_add_u32_e32 v84, 0x4000, v109
	v_lshl_add_u64 v[82:83], v[106:107], 0, s[8:9]
	v_readfirstlane_b32 s8, v84
	s_mov_b32 m0, s8
	s_nop 0
	global_load_lds_dwordx4 v[82:83], off
.LBB3_83:
	v_add_u32_e32 v82, s18, v115
	v_add_u32_e32 v118, 0x5000, v82
	v_or_b32_e32 v115, v118, v116
	v_add_u32_e32 v124, 0, v115
	ds_read_b128 v[86:89], v124 offset:53248
	ds_read_b128 v[90:93], v124 offset:55296
	ds_read_b128 v[82:85], v136 offset:53248
	ds_read_b128 v[138:141], v136 offset:55296
	s_and_b64 vcc, exec, s[4:5]
	s_waitcnt lgkmcnt(0)
	v_mfma_f32_16x16x32_f16 v[18:21], v[86:89], v[82:85], v[18:21]
	s_mov_b32 m0, s76
	v_mfma_f32_16x16x32_f16 v[22:25], v[90:93], v[82:85], v[22:25]
	global_load_lds_dwordx4 v168, s[72:73]
	v_mfma_f32_16x16x32_f16 v[26:29], v[86:89], v[138:141], v[26:29]
	s_mov_b32 m0, s77
	v_mfma_f32_16x16x32_f16 v[30:33], v[90:93], v[138:141], v[30:33]
	global_load_lds_dwordx4 v169, s[72:73]
	ds_read_b128 v[82:85], v136 offset:57344
	ds_read_b128 v[138:141], v136 offset:59392
	s_waitcnt lgkmcnt(0)
	v_mfma_f32_16x16x32_f16 v[34:37], v[86:89], v[82:85], v[34:37]
	s_mov_b32 m0, s78
	v_mfma_f32_16x16x32_f16 v[38:41], v[90:93], v[82:85], v[38:41]
	global_load_lds_dwordx4 v170, s[72:73]
	v_mfma_f32_16x16x32_f16 v[42:45], v[86:89], v[138:141], v[42:45]
	s_mov_b32 m0, s79
	v_mfma_f32_16x16x32_f16 v[46:49], v[90:93], v[138:141], v[46:49]
	global_load_lds_dwordx4 v171, s[72:73]
	ds_read_b128 v[82:85], v136 offset:61440
	ds_read_b128 v[140:143], v136 offset:63488
	v_add_u32_e32 v138, 0xd000, v136
	s_waitcnt lgkmcnt(0)
	v_mfma_f32_16x16x32_f16 v[50:53], v[86:89], v[82:85], v[50:53]
	s_mov_b32 m0, s80
	v_mfma_f32_16x16x32_f16 v[54:57], v[90:93], v[82:85], v[54:57]
	global_load_lds_dwordx4 v172, s[74:75]
	v_mfma_f32_16x16x32_f16 v[62:65], v[86:89], v[140:143], v[62:65]
	s_mov_b32 m0, s81
	v_mfma_f32_16x16x32_f16 v[82:85], v[90:93], v[140:143], v[58:61]
	global_load_lds_dwordx4 v173, s[74:75]
	s_nop 2
	ds_read_b128 v[58:61], v138 offset:12288
	ds_read_b128 v[140:143], v138 offset:14336
	s_waitcnt lgkmcnt(0)
	v_mfma_f32_16x16x32_f16 v[66:69], v[86:89], v[58:61], v[66:69]
	v_mfma_f32_16x16x32_f16 v[70:73], v[90:93], v[58:61], v[70:73]
	v_mfma_f32_16x16x32_f16 v[74:77], v[86:89], v[140:143], v[74:77]
	v_mfma_f32_16x16x32_f16 v[78:81], v[90:93], v[140:143], v[78:81]
	s_cbranch_vccnz .LBB3_85
	ds_read_b128 v[58:61], v138 offset:16384
	s_waitcnt lgkmcnt(0)
	v_mfma_f32_16x16x32_f16 v[10:13], v[86:89], v[58:61], v[10:13]
	v_mfma_f32_16x16x32_f16 v[14:17], v[90:93], v[58:61], v[14:17]

.LBB3_92:
	s_mov_b64 s[8:9], 0x200
	s_add_u32 s72, s66, 0x200
	s_addc_u32 s73, s67, 0
	s_add_u32 s74, s68, 0x200
	s_addc_u32 s75, s69, 0
	s_barrier
	s_waitcnt lgkmcnt(0)
	v_add_u32_e32 v90, s17, v115
	ds_read_b128 v[82:85], v90
	ds_read_b128 v[86:89], v90 offset:2048
	v_add_u32_e32 v125, s17, v113
	ds_read_b128 v[118:121], v125
	ds_read_b128 v[142:145], v125 offset:2048
	ds_read_b128 v[148:151], v125 offset:4096
	ds_read_b128 v[152:155], v125 offset:6144
	ds_read_b128 v[156:159], v125 offset:8192
	ds_read_b128 v[160:163], v125 offset:10240
	s_and_b64 vcc, exec, s[2:3]
	s_cbranch_vccnz .LBB3_94
	v_lshl_add_u64 v[164:165], v[106:107], 0, s[8:9]
	s_add_i32 s8, 0, 0x11000
	v_add_u32_e32 v166, s8, v108
	s_nop 0
	v_readfirstlane_b32 s8, v166
	s_mov_b32 m0, s8
	s_nop 0
	global_load_lds_dwordx4 v[164:165], off
.LBB3_94:
	s_and_b64 vcc, exec, s[4:5]
	s_waitcnt lgkmcnt(5)
	v_mfma_f32_16x16x32_f16 v[22:25], v[86:89], v[118:121], v[22:25]
	s_mov_b32 m0, s82
	v_mfma_f32_16x16x32_f16 v[18:21], v[82:85], v[118:121], v[18:21]
	global_load_lds_dwordx4 v168, s[72:73]
	s_waitcnt lgkmcnt(4)
	v_mfma_f32_16x16x32_f16 v[26:29], v[82:85], v[142:145], v[26:29]
	s_mov_b32 m0, s83
	v_mfma_f32_16x16x32_f16 v[30:33], v[86:89], v[142:145], v[30:33]
	global_load_lds_dwordx4 v169, s[72:73]
	s_waitcnt lgkmcnt(3)
	v_mfma_f32_16x16x32_f16 v[34:37], v[82:85], v[148:151], v[34:37]
	s_mov_b32 m0, s84
	v_mfma_f32_16x16x32_f16 v[38:41], v[86:89], v[148:151], v[38:41]
	global_load_lds_dwordx4 v170, s[72:73]
	ds_read_b128 v[148:151], v125 offset:12288
	s_waitcnt lgkmcnt(3)
	v_mfma_f32_16x16x32_f16 v[42:45], v[82:85], v[152:155], v[42:45]
	s_mov_b32 m0, s85
	v_mfma_f32_16x16x32_f16 v[46:49], v[86:89], v[152:155], v[46:49]
	global_load_lds_dwordx4 v171, s[72:73]
	ds_read_b128 v[152:155], v125 offset:14336
	s_waitcnt lgkmcnt(3)
	v_mfma_f32_16x16x32_f16 v[50:53], v[82:85], v[156:159], v[50:53]
	s_mov_b32 m0, s86
	v_mfma_f32_16x16x32_f16 v[54:57], v[86:89], v[156:159], v[54:57]
	global_load_lds_dwordx4 v172, s[74:75]
	s_waitcnt lgkmcnt(2)
	v_mfma_f32_16x16x32_f16 v[58:61], v[82:85], v[160:163], v[58:61]
	s_mov_b32 m0, s87
	v_mfma_f32_16x16x32_f16 v[62:65], v[86:89], v[160:163], v[62:65]
	global_load_lds_dwordx4 v173, s[74:75]
	s_waitcnt lgkmcnt(1)
	v_mfma_f32_16x16x32_f16 v[66:69], v[82:85], v[148:151], v[66:69]
	v_mfma_f32_16x16x32_f16 v[70:73], v[86:89], v[148:151], v[70:73]
	s_waitcnt lgkmcnt(0)
	v_mfma_f32_16x16x32_f16 v[74:77], v[82:85], v[152:155], v[74:77]
	v_mfma_f32_16x16x32_f16 v[78:81], v[86:89], v[152:155], v[78:81]
	s_cbranch_vccnz .LBB3_96
	ds_read_b128 v[118:121], v125 offset:16384
	s_waitcnt lgkmcnt(0)
	v_mfma_f32_16x16x32_f16 v[10:13], v[82:85], v[118:121], v[10:13]
	v_mfma_f32_16x16x32_f16 v[14:17], v[86:89], v[118:121], v[14:17]

.LBB3_106:
	s_mov_b64 s[10:11], 0x280
	s_add_u32 s72, s66, 0x280
	s_addc_u32 s73, s67, 0
	s_add_u32 s74, s68, 0x280
	s_addc_u32 s75, s69, 0
	s_barrier
	v_readfirstlane_b32 s12, v112
	s_and_b64 vcc, exec, s[2:3]
	s_cbranch_vccnz .LBB3_108
	v_lshl_add_u64 v[82:83], v[106:107], 0, s[10:11]
	s_add_i32 s10, 0, 0x1e000
	v_add_u32_e32 v84, s10, v108
	s_nop 0
	v_readfirstlane_b32 s10, v84
	s_mov_b32 m0, s10
	s_nop 0
	global_load_lds_dwordx4 v[82:83], off
.LBB3_108:
	s_waitcnt lgkmcnt(0)
	ds_read_b128 v[82:85], v122 offset:20480
	ds_read_b128 v[86:89], v122 offset:22528
	ds_read_b128 v[112:115], v136
	ds_read_b128 v[116:119], v136 offset:2048
	ds_read_b128 v[148:151], v136 offset:4096
	ds_read_b128 v[152:155], v136 offset:6144
	ds_read_b128 v[156:159], v136 offset:8192
	ds_read_b128 v[160:163], v136 offset:10240
	s_and_b64 vcc, exec, s[4:5]
	s_waitcnt lgkmcnt(5)
	v_mfma_f32_16x16x32_f16 v[18:21], v[82:85], v[112:115], v[18:21]
	s_mov_b32 m0, s88
	v_mfma_f32_16x16x32_f16 v[22:25], v[86:89], v[112:115], v[22:25]
	global_load_lds_dwordx4 v168, s[72:73]
	s_waitcnt lgkmcnt(4)
	v_mfma_f32_16x16x32_f16 v[26:29], v[82:85], v[116:119], v[26:29]
	s_mov_b32 m0, s89
	v_mfma_f32_16x16x32_f16 v[30:33], v[86:89], v[116:119], v[30:33]
	global_load_lds_dwordx4 v169, s[72:73]
	s_waitcnt lgkmcnt(3)
	v_mfma_f32_16x16x32_f16 v[34:37], v[82:85], v[148:151], v[34:37]
	s_mov_b32 m0, s90
	v_mfma_f32_16x16x32_f16 v[38:41], v[86:89], v[148:151], v[38:41]
	global_load_lds_dwordx4 v170, s[72:73]
	ds_read_b128 v[148:151], v136 offset:12288
	s_waitcnt lgkmcnt(3)
	v_mfma_f32_16x16x32_f16 v[42:45], v[82:85], v[152:155], v[42:45]
	s_mov_b32 m0, s91
	v_mfma_f32_16x16x32_f16 v[46:49], v[86:89], v[152:155], v[46:49]
	global_load_lds_dwordx4 v171, s[72:73]
	ds_read_b128 v[152:155], v136 offset:14336
	s_waitcnt lgkmcnt(3)
	v_mfma_f32_16x16x32_f16 v[50:53], v[82:85], v[156:159], v[50:53]
	s_mov_b32 m0, s92
	v_mfma_f32_16x16x32_f16 v[54:57], v[86:89], v[156:159], v[54:57]
	global_load_lds_dwordx4 v172, s[74:75]
	s_waitcnt lgkmcnt(2)
	v_mfma_f32_16x16x32_f16 v[58:61], v[82:85], v[160:163], v[58:61]
	s_mov_b32 m0, s93
	v_mfma_f32_16x16x32_f16 v[62:65], v[86:89], v[160:163], v[62:65]
	global_load_lds_dwordx4 v173, s[74:75]
	s_waitcnt lgkmcnt(1)
	v_mfma_f32_16x16x32_f16 v[66:69], v[82:85], v[148:151], v[66:69]
	v_mfma_f32_16x16x32_f16 v[70:73], v[86:89], v[148:151], v[70:73]
	s_waitcnt lgkmcnt(0)
	v_mfma_f32_16x16x32_f16 v[74:77], v[82:85], v[152:155], v[74:77]
	v_mfma_f32_16x16x32_f16 v[78:81], v[86:89], v[152:155], v[78:81]
	s_cbranch_vccnz .LBB3_110
	ds_read_b128 v[112:115], v136 offset:16384
	s_waitcnt lgkmcnt(0)
	v_mfma_f32_16x16x32_f16 v[10:13], v[82:85], v[112:115], v[10:13]
	v_mfma_f32_16x16x32_f16 v[14:17], v[86:89], v[112:115], v[14:17]

.LBB3_117:
	s_mov_b64 s[10:11], 0x300
	s_add_u32 s72, s66, 0x300
	s_addc_u32 s73, s67, 0
	s_add_u32 s74, s68, 0x300
	s_addc_u32 s75, s69, 0
	s_barrier
	s_waitcnt lgkmcnt(0)
	ds_read_b128 v[82:85], v124 offset:53248
	ds_read_b128 v[86:89], v124 offset:55296
	ds_read_b128 v[112:115], v136 offset:53248
	ds_read_b128 v[116:119], v136 offset:55296
	ds_read_b128 v[148:151], v136 offset:57344
	ds_read_b128 v[152:155], v136 offset:59392
	ds_read_b128 v[156:159], v136 offset:61440
	ds_read_b128 v[160:163], v136 offset:63488
	v_readfirstlane_b32 s12, v109
	s_and_b64 vcc, exec, s[2:3]
	s_cbranch_vccnz .LBB3_119
	v_add_u32_e32 v166, 0x4000, v109
	v_lshl_add_u64 v[164:165], v[106:107], 0, s[10:11]
	v_readfirstlane_b32 s10, v166
	s_mov_b32 m0, s10
	s_nop 0
	global_load_lds_dwordx4 v[164:165], off
.LBB3_119:
	s_and_b64 vcc, exec, s[4:5]
	s_waitcnt lgkmcnt(5)
	v_mfma_f32_16x16x32_f16 v[18:21], v[82:85], v[112:115], v[18:21]
	s_mov_b32 m0, s76
	v_mfma_f32_16x16x32_f16 v[22:25], v[86:89], v[112:115], v[22:25]
	global_load_lds_dwordx4 v168, s[72:73]
	s_waitcnt lgkmcnt(4)
	v_mfma_f32_16x16x32_f16 v[26:29], v[82:85], v[116:119], v[26:29]
	s_mov_b32 m0, s77
	v_mfma_f32_16x16x32_f16 v[30:33], v[86:89], v[116:119], v[30:33]
	global_load_lds_dwordx4 v169, s[72:73]
	s_waitcnt lgkmcnt(3)
	v_mfma_f32_16x16x32_f16 v[34:37], v[82:85], v[148:151], v[34:37]
	s_mov_b32 m0, s78
	v_mfma_f32_16x16x32_f16 v[38:41], v[86:89], v[148:151], v[38:41]
	global_load_lds_dwordx4 v170, s[72:73]
	ds_read_b128 v[148:151], v138 offset:12288
	s_waitcnt lgkmcnt(3)
	v_mfma_f32_16x16x32_f16 v[42:45], v[82:85], v[152:155], v[42:45]
	s_mov_b32 m0, s79
	v_mfma_f32_16x16x32_f16 v[46:49], v[86:89], v[152:155], v[46:49]
	global_load_lds_dwordx4 v171, s[72:73]
	ds_read_b128 v[152:155], v138 offset:14336
	s_waitcnt lgkmcnt(3)
	v_mfma_f32_16x16x32_f16 v[50:53], v[82:85], v[156:159], v[50:53]
	s_mov_b32 m0, s80
	v_mfma_f32_16x16x32_f16 v[54:57], v[86:89], v[156:159], v[54:57]
	global_load_lds_dwordx4 v172, s[74:75]
	s_waitcnt lgkmcnt(2)
	v_mfma_f32_16x16x32_f16 v[58:61], v[82:85], v[160:163], v[58:61]
	s_mov_b32 m0, s81
	v_mfma_f32_16x16x32_f16 v[62:65], v[86:89], v[160:163], v[62:65]
	global_load_lds_dwordx4 v173, s[74:75]
	s_waitcnt lgkmcnt(1)
	v_mfma_f32_16x16x32_f16 v[66:69], v[82:85], v[148:151], v[66:69]
	v_mfma_f32_16x16x32_f16 v[70:73], v[86:89], v[148:151], v[70:73]
	s_waitcnt lgkmcnt(0)
	v_mfma_f32_16x16x32_f16 v[74:77], v[82:85], v[152:155], v[74:77]
	v_mfma_f32_16x16x32_f16 v[78:81], v[86:89], v[152:155], v[78:81]
	s_cbranch_vccnz .LBB3_121
	ds_read_b128 v[112:115], v138 offset:16384
	s_waitcnt lgkmcnt(0)
	v_mfma_f32_16x16x32_f16 v[10:13], v[82:85], v[112:115], v[10:13]
	v_mfma_f32_16x16x32_f16 v[14:17], v[86:89], v[112:115], v[14:17]

.LBB3_128:
	s_mov_b64 s[10:11], 0x380
	s_add_u32 s72, s66, 0x380
	s_addc_u32 s73, s67, 0
	s_add_u32 s74, s68, 0x380
	s_addc_u32 s75, s69, 0
	s_barrier
	s_waitcnt lgkmcnt(0)
	ds_read_b128 v[114:117], v90
	ds_read_b128 v[118:121], v90 offset:2048
	ds_read_b128 v[82:85], v125
	ds_read_b128 v[86:89], v125 offset:2048
	ds_read_b128 v[148:151], v125 offset:4096
	ds_read_b128 v[152:155], v125 offset:6144
	ds_read_b128 v[156:159], v125 offset:8192
	ds_read_b128 v[160:163], v125 offset:10240
	s_and_b64 vcc, exec, s[2:3]
	s_cbranch_vccnz .LBB3_130
	s_add_i32 s2, 0, 0x11000
	v_add_u32_e32 v166, s2, v108
	v_lshl_add_u64 v[164:165], v[106:107], 0, s[10:11]
	v_readfirstlane_b32 s2, v166
	s_mov_b32 m0, s2
	s_nop 0
	global_load_lds_dwordx4 v[164:165], off
.LBB3_130:
	s_and_b64 vcc, exec, s[4:5]
	s_waitcnt lgkmcnt(5)
	v_mfma_f32_16x16x32_f16 v[18:21], v[114:117], v[82:85], v[18:21]
	s_mov_b32 m0, s82
	v_mfma_f32_16x16x32_f16 v[22:25], v[118:121], v[82:85], v[22:25]
	global_load_lds_dwordx4 v168, s[72:73]
	s_waitcnt lgkmcnt(4)
	v_mfma_f32_16x16x32_f16 v[26:29], v[114:117], v[86:89], v[26:29]
	s_mov_b32 m0, s83
	v_mfma_f32_16x16x32_f16 v[30:33], v[118:121], v[86:89], v[30:33]
	global_load_lds_dwordx4 v169, s[72:73]
	s_waitcnt lgkmcnt(2)
	v_mfma_f32_16x16x32_f16 v[42:45], v[114:117], v[152:155], v[42:45]
	s_mov_b32 m0, s84
	v_mfma_f32_16x16x32_f16 v[46:49], v[118:121], v[152:155], v[46:49]
	global_load_lds_dwordx4 v170, s[72:73]
	v_mfma_f32_16x16x32_f16 v[34:37], v[114:117], v[148:151], v[34:37]
	s_mov_b32 m0, s85
	v_mfma_f32_16x16x32_f16 v[38:41], v[118:121], v[148:151], v[38:41]
	global_load_lds_dwordx4 v171, s[72:73]
	ds_read_b128 v[148:151], v125 offset:12288
	ds_read_b128 v[152:155], v125 offset:14336
	s_waitcnt lgkmcnt(3)
	v_mfma_f32_16x16x32_f16 v[82:85], v[114:117], v[156:159], v[50:53]
	s_mov_b32 m0, s86
	v_mfma_f32_16x16x32_f16 v[86:89], v[118:121], v[156:159], v[54:57]
	global_load_lds_dwordx4 v172, s[74:75]
	s_nop 1
	s_waitcnt lgkmcnt(2)
	v_mfma_f32_16x16x32_f16 v[90:93], v[114:117], v[160:163], v[58:61]
	s_mov_b32 m0, s87
	v_mfma_f32_16x16x32_f16 v[94:97], v[118:121], v[160:163], v[62:65]
	global_load_lds_dwordx4 v173, s[74:75]
	s_waitcnt lgkmcnt(1)
	v_mfma_f32_16x16x32_f16 v[98:101], v[114:117], v[148:151], v[66:69]
	v_mfma_f32_16x16x32_f16 v[102:105], v[118:121], v[148:151], v[70:73]
	s_waitcnt lgkmcnt(0)
	v_mfma_f32_16x16x32_f16 v[106:109], v[114:117], v[152:155], v[74:77]
	v_mfma_f32_16x16x32_f16 v[110:113], v[118:121], v[152:155], v[78:81]
	s_cbranch_vccnz .LBB3_132
	ds_read_b128 v[50:53], v125 offset:16384
	s_waitcnt lgkmcnt(0)
	v_mfma_f32_16x16x32_f16 v[10:13], v[114:117], v[50:53], v[10:13]
	v_mfma_f32_16x16x32_f16 v[14:17], v[118:121], v[50:53], v[14:17]

.LBB4_85:
	s_add_i32 s27, 0, 0x1f000
	v_add_u32_e32 v144, s27, v1
	s_mov_b64 s[24:25], 0x100
	v_readfirstlane_b32 s27, v144
	v_add_u32_e32 v23, 0x2000, v144
	v_lshl_add_u64 v[34:35], v[116:117], 0, s[24:25]
	s_mov_b32 m0, s27
	v_readfirstlane_b32 s27, v23
	v_add_u32_e32 v23, 0x4000, v144
	v_readfirstlane_b32 s70, v0
	s_nop 3
	s_lshr_b32 s70, s70, 6
	s_lshl_b32 s70, s70, 10
	s_add_i32 s76, s70, 0x5000
	s_add_i32 s77, s70, 0x7000
	s_add_i32 s78, s70, 0x9000
	s_add_i32 s79, s70, 0xb000
	s_add_i32 s80, s70, 0x0
	s_add_i32 s81, s70, 0x2000
	s_add_i32 s82, s70, 0x12000
	s_add_i32 s83, s70, 0x14000
	s_add_i32 s84, s70, 0x16000
	s_add_i32 s85, s70, 0x18000
	s_add_i32 s86, s70, 0xd000
	s_add_i32 s87, s70, 0xf000
	s_add_i32 s88, s70, 0x1f000
	s_add_i32 s89, s70, 0x21000
	s_add_i32 s90, s70, 0x23000
	s_add_i32 s91, s70, 0x25000
	s_add_i32 s92, s70, 0x1a000
	s_add_i32 s93, s70, 0x1c000
	v_subrev_u32_e32 v176, s66, v116
	v_subrev_u32_e32 v177, s66, v114
	v_subrev_u32_e32 v178, s66, v112
	v_subrev_u32_e32 v179, s66, v110
	v_subrev_u32_e32 v180, s68, v120
	v_subrev_u32_e32 v181, s68, v118
	s_add_u32 s72, s66, 0x100
	s_addc_u32 s73, s67, 0
	s_add_u32 s74, s68, 0x100
	s_addc_u32 s75, s69, 0
	s_barrier
	s_add_i32 s35, 0, 0x1a000
	v_add_u32_e32 v145, s35, v1
	v_readfirstlane_b32 s27, v145
	s_and_b64 vcc, exec, s[14:15]
	s_cbranch_vccnz .LBB4_87
	v_lshl_add_u64 v[34:35], v[122:123], 0, s[24:25]
	s_add_i32 s24, 0, 0x1e000
	v_add_u32_e32 v23, s24, v1
	s_nop 0
	v_readfirstlane_b32 s24, v23
	s_mov_b32 m0, s24
	s_nop 0
	global_load_lds_dwordx4 v[34:35], off
.LBB4_87:
	v_lshlrev_b32_e32 v140, 7, v42
	s_lshl_b32 s36, s26, 12
	v_bitop3_b32 v23, v102, v0, 7 bitop3:0x78
	v_lshlrev_b32_e32 v141, 4, v23
	v_or_b32_e32 v34, s36, v140
	v_or_b32_e32 v23, v34, v141
	v_add_u32_e32 v138, 0, v23
	ds_read_b128 v[50:53], v138 offset:20480
	v_or_b32_e32 v146, v141, v140
	v_add_u32_e32 v137, 0, v146
	ds_read_b128 v[58:61], v137
	ds_read_b128 v[62:65], v138 offset:22528
	v_cvt_f32_f16_sdwa v45, v43 dst_sel:DWORD dst_unused:UNUSED_PAD src0_sel:WORD_1
	v_cvt_f32_f16_e32 v44, v43
	v_cvt_f32_f16_sdwa v47, v6 dst_sel:DWORD dst_unused:UNUSED_PAD src0_sel:WORD_1
	v_cvt_f32_f16_e32 v46, v6
	v_cvt_f32_f16_sdwa v55, v8 dst_sel:DWORD dst_unused:UNUSED_PAD src0_sel:WORD_1
	v_cvt_f32_f16_e32 v54, v8
	v_cvt_f32_f16_sdwa v57, v9 dst_sel:DWORD dst_unused:UNUSED_PAD src0_sel:WORD_1
	v_cvt_f32_f16_e32 v56, v9
	ds_read_b128 v[66:69], v137 offset:2048
	ds_read_b128 v[70:73], v137 offset:4096
	s_waitcnt lgkmcnt(0)
	v_mfma_f32_16x16x32_f16 v[42:45], v[50:53], v[58:61], v[44:47]
	v_cvt_f32_f16_sdwa v79, v12 dst_sel:DWORD dst_unused:UNUSED_PAD src0_sel:WORD_1
	v_cvt_f32_f16_e32 v78, v12
	v_cvt_f32_f16_sdwa v81, v13 dst_sel:DWORD dst_unused:UNUSED_PAD src0_sel:WORD_1
	s_mov_b32 m0, s88
	v_mfma_f32_16x16x32_f16 v[46:49], v[62:65], v[58:61], v[54:57]
	global_load_lds_dwordx4 v176, s[72:73]
	v_cvt_f32_f16_sdwa v59, v4 dst_sel:DWORD dst_unused:UNUSED_PAD src0_sel:WORD_1
	v_cvt_f32_f16_e32 v58, v4
	v_cvt_f32_f16_sdwa v61, v5 dst_sel:DWORD dst_unused:UNUSED_PAD src0_sel:WORD_1
	v_cvt_f32_f16_sdwa v55, v2 dst_sel:DWORD dst_unused:UNUSED_PAD src0_sel:WORD_1
	v_cvt_f32_f16_e32 v54, v2
	v_cvt_f32_f16_sdwa v57, v3 dst_sel:DWORD dst_unused:UNUSED_PAD src0_sel:WORD_1
	v_cvt_f32_f16_e32 v56, v3
	v_cvt_f32_f16_e32 v60, v5
	v_cvt_f32_f16_sdwa v3, v16 dst_sel:DWORD dst_unused:UNUSED_PAD src0_sel:WORD_1
	v_mfma_f32_16x16x32_f16 v[54:57], v[50:53], v[66:69], v[54:57]
	v_cvt_f32_f16_e32 v2, v16
	v_cvt_f32_f16_sdwa v5, v17 dst_sel:DWORD dst_unused:UNUSED_PAD src0_sel:WORD_1
	v_cvt_f32_f16_e32 v4, v17
	s_mov_b32 m0, s89
	v_mfma_f32_16x16x32_f16 v[58:61], v[62:65], v[66:69], v[58:61]
	global_load_lds_dwordx4 v177, s[72:73]
	v_cvt_f32_f16_sdwa v67, v14 dst_sel:DWORD dst_unused:UNUSED_PAD src0_sel:WORD_1
	v_cvt_f32_f16_e32 v66, v14
	v_cvt_f32_f16_sdwa v69, v7 dst_sel:DWORD dst_unused:UNUSED_PAD src0_sel:WORD_1
	v_cvt_f32_f16_e32 v68, v7
	ds_read_b128 v[6:9], v137 offset:6144
	v_cvt_f32_f16_e32 v80, v13
	v_mfma_f32_16x16x32_f16 v[66:69], v[50:53], v[70:73], v[66:69]
	v_cvt_f32_f16_sdwa v99, v28 dst_sel:DWORD dst_unused:UNUSED_PAD src0_sel:WORD_1
	v_cvt_f32_f16_e32 v98, v28
	v_cvt_f32_f16_sdwa v101, v29 dst_sel:DWORD dst_unused:UNUSED_PAD src0_sel:WORD_1
	s_mov_b32 m0, s90
	v_mfma_f32_16x16x32_f16 v[70:73], v[62:65], v[70:73], v[2:5]
	global_load_lds_dwordx4 v178, s[72:73]
	v_cvt_f32_f16_e32 v100, v29
	s_cmpk_gt_u32 s34, 0x8f
	s_cselect_b64 s[26:27], -1, 0
	v_cvt_f32_f16_sdwa v3, v10 dst_sel:DWORD dst_unused:UNUSED_PAD src0_sel:WORD_1
	v_cvt_f32_f16_e32 v2, v10
	v_cvt_f32_f16_sdwa v5, v11 dst_sel:DWORD dst_unused:UNUSED_PAD src0_sel:WORD_1
	v_cvt_f32_f16_e32 v4, v11
	ds_read_b128 v[10:13], v137 offset:8192
	s_waitcnt lgkmcnt(0)
	v_mfma_f32_16x16x32_f16 v[78:81], v[62:65], v[6:9], v[78:81]
	s_cmpk_lt_u32 s34, 0x90
	s_mov_b32 m0, s91
	v_mfma_f32_16x16x32_f16 v[74:77], v[50:53], v[6:9], v[2:5]
	global_load_lds_dwordx4 v179, s[72:73]
	v_cvt_f32_f16_sdwa v7, v22 dst_sel:DWORD dst_unused:UNUSED_PAD src0_sel:WORD_1
	v_cvt_f32_f16_e32 v6, v22
	v_cvt_f32_f16_sdwa v9, v15 dst_sel:DWORD dst_unused:UNUSED_PAD src0_sel:WORD_1
	v_cvt_f32_f16_sdwa v3, v24 dst_sel:DWORD dst_unused:UNUSED_PAD src0_sel:WORD_1
	v_cvt_f32_f16_e32 v2, v24
	v_cvt_f32_f16_sdwa v5, v25 dst_sel:DWORD dst_unused:UNUSED_PAD src0_sel:WORD_1
	v_cvt_f32_f16_e32 v4, v25
	v_cvt_f32_f16_e32 v8, v15
	ds_read_b128 v[14:17], v137 offset:10240
	v_mfma_f32_16x16x32_f16 v[22:25], v[62:65], v[10:13], v[2:5]
	s_nop 2
	v_cvt_f32_f16_sdwa v3, v18 dst_sel:DWORD dst_unused:UNUSED_PAD src0_sel:WORD_1
	v_cvt_f32_f16_e32 v2, v18
	v_cvt_f32_f16_sdwa v5, v19 dst_sel:DWORD dst_unused:UNUSED_PAD src0_sel:WORD_1
	v_cvt_f32_f16_e32 v4, v19
	s_mov_b32 m0, s92
	v_mfma_f32_16x16x32_f16 v[82:85], v[50:53], v[10:13], v[6:9]
	global_load_lds_dwordx4 v180, s[74:75]
	ds_read_b128 v[10:13], v137 offset:12288
	s_nop 1
	v_cvt_f32_f16_sdwa v7, v20 dst_sel:DWORD dst_unused:UNUSED_PAD src0_sel:WORD_1
	v_cvt_f32_f16_e32 v6, v20
	v_cvt_f32_f16_sdwa v9, v21 dst_sel:DWORD dst_unused:UNUSED_PAD src0_sel:WORD_1
	v_cvt_f32_f16_e32 v8, v21
	s_waitcnt lgkmcnt(0)
	v_mfma_f32_16x16x32_f16 v[86:89], v[50:53], v[14:17], v[2:5]
	s_nop 2
	v_cvt_f32_f16_sdwa v3, v32 dst_sel:DWORD dst_unused:UNUSED_PAD src0_sel:WORD_1
	v_cvt_f32_f16_e32 v2, v32
	v_cvt_f32_f16_sdwa v5, v33 dst_sel:DWORD dst_unused:UNUSED_PAD src0_sel:WORD_1
	v_cvt_f32_f16_e32 v4, v33
	s_mov_b32 m0, s93
	v_mfma_f32_16x16x32_f16 v[18:21], v[62:65], v[14:17], v[6:9]
	global_load_lds_dwordx4 v181, s[74:75]
	ds_read_b128 v[14:17], v137 offset:14336
	s_nop 1
	v_cvt_f32_f16_sdwa v7, v90 dst_sel:DWORD dst_unused:UNUSED_PAD src0_sel:WORD_1
	v_cvt_f32_f16_e32 v6, v90
	v_cvt_f32_f16_sdwa v9, v30 dst_sel:DWORD dst_unused:UNUSED_PAD src0_sel:WORD_1
	v_cvt_f32_f16_e32 v8, v30
	v_mfma_f32_16x16x32_f16 v[30:33], v[62:65], v[10:13], v[2:5]
	s_nop 2
	v_cvt_f32_f16_sdwa v3, v26 dst_sel:DWORD dst_unused:UNUSED_PAD src0_sel:WORD_1
	v_cvt_f32_f16_e32 v2, v26
	v_cvt_f32_f16_sdwa v5, v27 dst_sel:DWORD dst_unused:UNUSED_PAD src0_sel:WORD_1
	v_cvt_f32_f16_e32 v4, v27
	v_mfma_f32_16x16x32_f16 v[90:93], v[50:53], v[10:13], v[6:9]
	s_waitcnt lgkmcnt(0)
	v_mfma_f32_16x16x32_f16 v[94:97], v[50:53], v[14:17], v[2:5]
	s_nop 0
	v_cvt_f32_f16_sdwa v7, v38 dst_sel:DWORD dst_unused:UNUSED_PAD src0_sel:WORD_1
	v_cvt_f32_f16_e32 v6, v38
	v_cvt_f32_f16_sdwa v9, v39 dst_sel:DWORD dst_unused:UNUSED_PAD src0_sel:WORD_1
	v_cvt_f32_f16_sdwa v3, v40 dst_sel:DWORD dst_unused:UNUSED_PAD src0_sel:WORD_1
	v_cvt_f32_f16_e32 v2, v40
	v_cvt_f32_f16_sdwa v5, v41 dst_sel:DWORD dst_unused:UNUSED_PAD src0_sel:WORD_1
	v_cvt_f32_f16_e32 v4, v41
	v_cvt_f32_f16_e32 v8, v39
	v_mfma_f32_16x16x32_f16 v[98:101], v[62:65], v[14:17], v[98:101]
	s_cbranch_scc1 .LBB4_89
	ds_read_b128 v[10:13], v137 offset:16384
	s_waitcnt lgkmcnt(0)
	v_mfma_f32_16x16x32_f16 v[6:9], v[50:53], v[10:13], v[6:9]
	v_mfma_f32_16x16x32_f16 v[2:5], v[62:65], v[10:13], v[2:5]

.LBB4_96:
	s_mov_b64 s[28:29], 0x180
	s_add_u32 s72, s66, 0x180
	s_addc_u32 s73, s67, 0
	s_add_u32 s74, s68, 0x180
	s_addc_u32 s75, s69, 0
	s_barrier
	v_readfirstlane_b32 s34, v135
	s_and_b64 vcc, exec, s[14:15]
	s_cbranch_vccnz .LBB4_98
	v_add_u32_e32 v84, 0x4000, v135
	v_lshl_add_u64 v[82:83], v[122:123], 0, s[28:29]
	v_readfirstlane_b32 s28, v84
	s_mov_b32 m0, s28
	s_nop 0
	global_load_lds_dwordx4 v[82:83], off
.LBB4_98:
	v_add_u32_e32 v82, s36, v140
	v_add_u32_e32 v107, 0x5000, v82
	v_or_b32_e32 v106, v107, v141
	v_add_u32_e32 v142, 0, v106
	ds_read_b128 v[98:101], v142 offset:53248
	ds_read_b128 v[102:105], v142 offset:55296
	ds_read_b128 v[82:85], v137 offset:53248
	ds_read_b128 v[86:89], v137 offset:55296
	v_add_u32_e32 v140, 0xd000, v137
	s_and_b64 vcc, exec, s[24:25]
	s_waitcnt lgkmcnt(0)
	v_mfma_f32_16x16x32_f16 v[34:37], v[98:101], v[82:85], v[34:37]
	s_mov_b32 m0, s76
	v_mfma_f32_16x16x32_f16 v[38:41], v[102:105], v[82:85], v[38:41]
	global_load_lds_dwordx4 v176, s[72:73]
	v_mfma_f32_16x16x32_f16 v[42:45], v[98:101], v[86:89], v[42:45]
	s_mov_b32 m0, s77
	v_mfma_f32_16x16x32_f16 v[46:49], v[102:105], v[86:89], v[46:49]
	global_load_lds_dwordx4 v177, s[72:73]
	ds_read_b128 v[82:85], v137 offset:57344
	ds_read_b128 v[86:89], v137 offset:59392
	s_waitcnt lgkmcnt(0)
	v_mfma_f32_16x16x32_f16 v[50:53], v[98:101], v[82:85], v[50:53]
	s_mov_b32 m0, s78
	v_mfma_f32_16x16x32_f16 v[54:57], v[102:105], v[82:85], v[54:57]
	global_load_lds_dwordx4 v178, s[72:73]
	v_mfma_f32_16x16x32_f16 v[58:61], v[98:101], v[86:89], v[58:61]
	s_mov_b32 m0, s79
	v_mfma_f32_16x16x32_f16 v[62:65], v[102:105], v[86:89], v[62:65]
	global_load_lds_dwordx4 v179, s[72:73]
	ds_read_b128 v[82:85], v137 offset:61440
	ds_read_b128 v[86:89], v137 offset:63488
	s_waitcnt lgkmcnt(0)
	v_mfma_f32_16x16x32_f16 v[66:69], v[98:101], v[82:85], v[66:69]
	s_mov_b32 m0, s80
	v_mfma_f32_16x16x32_f16 v[70:73], v[102:105], v[82:85], v[70:73]
	global_load_lds_dwordx4 v180, s[74:75]
	v_mfma_f32_16x16x32_f16 v[82:85], v[102:105], v[86:89], v[18:21]
	s_nop 2
	ds_read_b128 v[18:21], v140 offset:12288
	ds_read_b128 v[148:151], v140 offset:14336
	s_mov_b32 m0, s81
	v_mfma_f32_16x16x32_f16 v[74:77], v[98:101], v[86:89], v[74:77]
	global_load_lds_dwordx4 v181, s[74:75]
	s_waitcnt lgkmcnt(0)
	v_mfma_f32_16x16x32_f16 v[86:89], v[98:101], v[18:21], v[22:25]
	v_mfma_f32_16x16x32_f16 v[90:93], v[102:105], v[18:21], v[26:29]
	v_mfma_f32_16x16x32_f16 v[94:97], v[98:101], v[148:151], v[30:33]
	v_mfma_f32_16x16x32_f16 v[78:81], v[102:105], v[148:151], v[78:81]
	s_cbranch_vccnz .LBB4_100
	ds_read_b128 v[18:21], v140 offset:16384
	s_waitcnt lgkmcnt(0)
	v_mfma_f32_16x16x32_f16 v[6:9], v[98:101], v[18:21], v[6:9]
	v_mfma_f32_16x16x32_f16 v[2:5], v[102:105], v[18:21], v[2:5]

.LBB4_107:
	s_mov_b64 s[28:29], 0x200
	s_add_u32 s72, s66, 0x200
	s_addc_u32 s73, s67, 0
	s_add_u32 s74, s68, 0x200
	s_addc_u32 s75, s69, 0
	s_barrier
	s_waitcnt lgkmcnt(0)
	v_add_u32_e32 v90, s35, v106
	ds_read_b128 v[82:85], v90
	ds_read_b128 v[86:89], v90 offset:2048
	v_add_u32_e32 v146, s35, v146
	ds_read_b128 v[92:95], v146
	ds_read_b128 v[96:99], v146 offset:2048
	ds_read_b128 v[156:159], v146 offset:4096
	ds_read_b128 v[160:163], v146 offset:6144
	ds_read_b128 v[164:167], v146 offset:8192
	ds_read_b128 v[168:171], v146 offset:10240
	s_and_b64 vcc, exec, s[14:15]
	s_cbranch_vccnz .LBB4_109
	v_lshl_add_u64 v[172:173], v[122:123], 0, s[28:29]
	s_add_i32 s28, 0, 0x11000
	v_add_u32_e32 v174, s28, v1
	s_nop 0
	v_readfirstlane_b32 s28, v174
	s_mov_b32 m0, s28
	s_nop 0
	global_load_lds_dwordx4 v[172:173], off
.LBB4_109:
	s_and_b64 vcc, exec, s[24:25]
	s_waitcnt lgkmcnt(5)
	v_mfma_f32_16x16x32_f16 v[22:25], v[86:89], v[92:95], v[22:25]
	s_mov_b32 m0, s82
	v_mfma_f32_16x16x32_f16 v[18:21], v[82:85], v[92:95], v[18:21]
	global_load_lds_dwordx4 v176, s[72:73]
	s_waitcnt lgkmcnt(4)
	v_mfma_f32_16x16x32_f16 v[26:29], v[82:85], v[96:99], v[26:29]
	s_mov_b32 m0, s83
	v_mfma_f32_16x16x32_f16 v[30:33], v[86:89], v[96:99], v[30:33]
	global_load_lds_dwordx4 v177, s[72:73]
	s_waitcnt lgkmcnt(3)
	v_mfma_f32_16x16x32_f16 v[34:37], v[82:85], v[156:159], v[34:37]
	s_mov_b32 m0, s84
	v_mfma_f32_16x16x32_f16 v[38:41], v[86:89], v[156:159], v[38:41]
	global_load_lds_dwordx4 v178, s[72:73]
	ds_read_b128 v[156:159], v146 offset:12288
	s_waitcnt lgkmcnt(3)
	v_mfma_f32_16x16x32_f16 v[42:45], v[82:85], v[160:163], v[42:45]
	s_mov_b32 m0, s85
	v_mfma_f32_16x16x32_f16 v[46:49], v[86:89], v[160:163], v[46:49]
	global_load_lds_dwordx4 v179, s[72:73]
	ds_read_b128 v[160:163], v146 offset:14336
	s_waitcnt lgkmcnt(3)
	v_mfma_f32_16x16x32_f16 v[50:53], v[82:85], v[164:167], v[50:53]
	s_mov_b32 m0, s86
	v_mfma_f32_16x16x32_f16 v[54:57], v[86:89], v[164:167], v[54:57]
	global_load_lds_dwordx4 v180, s[74:75]
	s_waitcnt lgkmcnt(2)
	v_mfma_f32_16x16x32_f16 v[58:61], v[82:85], v[168:171], v[58:61]
	s_mov_b32 m0, s87
	v_mfma_f32_16x16x32_f16 v[62:65], v[86:89], v[168:171], v[62:65]
	global_load_lds_dwordx4 v181, s[74:75]
	s_waitcnt lgkmcnt(1)
	v_mfma_f32_16x16x32_f16 v[66:69], v[82:85], v[156:159], v[66:69]
	v_mfma_f32_16x16x32_f16 v[70:73], v[86:89], v[156:159], v[70:73]
	s_waitcnt lgkmcnt(0)
	v_mfma_f32_16x16x32_f16 v[74:77], v[82:85], v[160:163], v[74:77]
	v_mfma_f32_16x16x32_f16 v[78:81], v[86:89], v[160:163], v[78:81]
	s_cbranch_vccnz .LBB4_111
	ds_read_b128 v[92:95], v146 offset:16384
	s_waitcnt lgkmcnt(0)
	v_mfma_f32_16x16x32_f16 v[6:9], v[82:85], v[92:95], v[6:9]
	v_mfma_f32_16x16x32_f16 v[2:5], v[86:89], v[92:95], v[2:5]

.LBB4_121:
	s_mov_b64 s[30:31], 0x280
	s_add_u32 s72, s66, 0x280
	s_addc_u32 s73, s67, 0
	s_add_u32 s74, s68, 0x280
	s_addc_u32 s75, s69, 0
	s_barrier
	s_waitcnt lgkmcnt(0)
	ds_read_b128 v[82:85], v138 offset:20480
	ds_read_b128 v[86:89], v138 offset:22528
	ds_read_b128 v[92:95], v137
	ds_read_b128 v[96:99], v137 offset:2048
	ds_read_b128 v[156:159], v137 offset:4096
	ds_read_b128 v[160:163], v137 offset:6144
	ds_read_b128 v[164:167], v137 offset:8192
	ds_read_b128 v[168:171], v137 offset:10240
	v_readfirstlane_b32 s34, v145
	s_and_b64 vcc, exec, s[14:15]
	s_cbranch_vccnz .LBB4_123
	v_lshl_add_u64 v[172:173], v[122:123], 0, s[30:31]
	s_add_i32 s30, 0, 0x1e000
	v_add_u32_e32 v174, s30, v1
	s_nop 0
	v_readfirstlane_b32 s30, v174
	s_mov_b32 m0, s30
	s_nop 0
	global_load_lds_dwordx4 v[172:173], off
.LBB4_123:
	s_and_b64 vcc, exec, s[24:25]
	s_waitcnt lgkmcnt(5)
	v_mfma_f32_16x16x32_f16 v[18:21], v[82:85], v[92:95], v[18:21]
	s_mov_b32 m0, s88
	v_mfma_f32_16x16x32_f16 v[22:25], v[86:89], v[92:95], v[22:25]
	global_load_lds_dwordx4 v176, s[72:73]
	s_waitcnt lgkmcnt(4)
	v_mfma_f32_16x16x32_f16 v[26:29], v[82:85], v[96:99], v[26:29]
	s_mov_b32 m0, s89
	v_mfma_f32_16x16x32_f16 v[30:33], v[86:89], v[96:99], v[30:33]
	global_load_lds_dwordx4 v177, s[72:73]
	s_waitcnt lgkmcnt(3)
	v_mfma_f32_16x16x32_f16 v[34:37], v[82:85], v[156:159], v[34:37]
	s_mov_b32 m0, s90
	v_mfma_f32_16x16x32_f16 v[38:41], v[86:89], v[156:159], v[38:41]
	global_load_lds_dwordx4 v178, s[72:73]
	ds_read_b128 v[156:159], v137 offset:12288
	s_waitcnt lgkmcnt(3)
	v_mfma_f32_16x16x32_f16 v[42:45], v[82:85], v[160:163], v[42:45]
	s_mov_b32 m0, s91
	v_mfma_f32_16x16x32_f16 v[46:49], v[86:89], v[160:163], v[46:49]
	global_load_lds_dwordx4 v179, s[72:73]
	ds_read_b128 v[160:163], v137 offset:14336
	s_waitcnt lgkmcnt(3)
	v_mfma_f32_16x16x32_f16 v[50:53], v[82:85], v[164:167], v[50:53]
	s_mov_b32 m0, s92
	v_mfma_f32_16x16x32_f16 v[54:57], v[86:89], v[164:167], v[54:57]
	global_load_lds_dwordx4 v180, s[74:75]
	s_waitcnt lgkmcnt(2)
	v_mfma_f32_16x16x32_f16 v[58:61], v[82:85], v[168:171], v[58:61]
	s_mov_b32 m0, s93
	v_mfma_f32_16x16x32_f16 v[62:65], v[86:89], v[168:171], v[62:65]
	global_load_lds_dwordx4 v181, s[74:75]
	s_waitcnt lgkmcnt(1)
	v_mfma_f32_16x16x32_f16 v[66:69], v[82:85], v[156:159], v[66:69]
	v_mfma_f32_16x16x32_f16 v[70:73], v[86:89], v[156:159], v[70:73]
	s_waitcnt lgkmcnt(0)
	v_mfma_f32_16x16x32_f16 v[74:77], v[82:85], v[160:163], v[74:77]
	v_mfma_f32_16x16x32_f16 v[78:81], v[86:89], v[160:163], v[78:81]
	s_cbranch_vccnz .LBB4_125
	ds_read_b128 v[92:95], v137 offset:16384
	s_waitcnt lgkmcnt(0)
	v_mfma_f32_16x16x32_f16 v[6:9], v[82:85], v[92:95], v[6:9]
	v_mfma_f32_16x16x32_f16 v[2:5], v[86:89], v[92:95], v[2:5]

.LBB4_132:
	s_mov_b64 s[30:31], 0x300
	s_add_u32 s72, s66, 0x300
	s_addc_u32 s73, s67, 0
	s_add_u32 s74, s68, 0x300
	s_addc_u32 s75, s69, 0
	s_barrier
	s_waitcnt lgkmcnt(0)
	ds_read_b128 v[82:85], v142 offset:53248
	ds_read_b128 v[86:89], v142 offset:55296
	ds_read_b128 v[92:95], v137 offset:53248
	ds_read_b128 v[96:99], v137 offset:55296
	ds_read_b128 v[156:159], v137 offset:57344
	ds_read_b128 v[160:163], v137 offset:59392
	ds_read_b128 v[164:167], v137 offset:61440
	ds_read_b128 v[168:171], v137 offset:63488
	v_readfirstlane_b32 s34, v135
	s_and_b64 vcc, exec, s[14:15]
	s_cbranch_vccnz .LBB4_134
	v_add_u32_e32 v174, 0x4000, v135
	v_lshl_add_u64 v[172:173], v[122:123], 0, s[30:31]
	v_readfirstlane_b32 s30, v174
	s_mov_b32 m0, s30
	s_nop 0
	global_load_lds_dwordx4 v[172:173], off
.LBB4_134:
	s_and_b64 vcc, exec, s[24:25]
	s_waitcnt lgkmcnt(5)
	v_mfma_f32_16x16x32_f16 v[18:21], v[82:85], v[92:95], v[18:21]
	s_mov_b32 m0, s76
	v_mfma_f32_16x16x32_f16 v[22:25], v[86:89], v[92:95], v[22:25]
	global_load_lds_dwordx4 v176, s[72:73]
	s_waitcnt lgkmcnt(4)
	v_mfma_f32_16x16x32_f16 v[26:29], v[82:85], v[96:99], v[26:29]
	s_mov_b32 m0, s77
	v_mfma_f32_16x16x32_f16 v[30:33], v[86:89], v[96:99], v[30:33]
	global_load_lds_dwordx4 v177, s[72:73]
	s_waitcnt lgkmcnt(3)
	v_mfma_f32_16x16x32_f16 v[34:37], v[82:85], v[156:159], v[34:37]
	s_mov_b32 m0, s78
	v_mfma_f32_16x16x32_f16 v[38:41], v[86:89], v[156:159], v[38:41]
	global_load_lds_dwordx4 v178, s[72:73]
	ds_read_b128 v[156:159], v140 offset:12288
	s_waitcnt lgkmcnt(3)
	v_mfma_f32_16x16x32_f16 v[42:45], v[82:85], v[160:163], v[42:45]
	s_mov_b32 m0, s79
	v_mfma_f32_16x16x32_f16 v[46:49], v[86:89], v[160:163], v[46:49]
	global_load_lds_dwordx4 v179, s[72:73]
	ds_read_b128 v[160:163], v140 offset:14336
	s_waitcnt lgkmcnt(3)
	v_mfma_f32_16x16x32_f16 v[50:53], v[82:85], v[164:167], v[50:53]
	s_mov_b32 m0, s80
	v_mfma_f32_16x16x32_f16 v[54:57], v[86:89], v[164:167], v[54:57]
	global_load_lds_dwordx4 v180, s[74:75]
	s_waitcnt lgkmcnt(2)
	v_mfma_f32_16x16x32_f16 v[58:61], v[82:85], v[168:171], v[58:61]
	s_mov_b32 m0, s81
	v_mfma_f32_16x16x32_f16 v[62:65], v[86:89], v[168:171], v[62:65]
	global_load_lds_dwordx4 v181, s[74:75]
	s_waitcnt lgkmcnt(1)
	v_mfma_f32_16x16x32_f16 v[66:69], v[82:85], v[156:159], v[66:69]
	v_mfma_f32_16x16x32_f16 v[70:73], v[86:89], v[156:159], v[70:73]
	s_waitcnt lgkmcnt(0)
	v_mfma_f32_16x16x32_f16 v[74:77], v[82:85], v[160:163], v[74:77]
	v_mfma_f32_16x16x32_f16 v[78:81], v[86:89], v[160:163], v[78:81]
	s_cbranch_vccnz .LBB4_136
	ds_read_b128 v[92:95], v140 offset:16384
	s_waitcnt lgkmcnt(0)
	v_mfma_f32_16x16x32_f16 v[6:9], v[82:85], v[92:95], v[6:9]
	v_mfma_f32_16x16x32_f16 v[2:5], v[86:89], v[92:95], v[2:5]

.LBB4_143:
	s_mov_b64 s[30:31], 0x380
	v_add_u32_e32 v84, 0x2000, v136
	v_add_u32_e32 v84, 0x4000, v136
	s_add_u32 s72, s66, 0x380
	s_addc_u32 s73, s67, 0
	s_add_u32 s74, s68, 0x380
	s_addc_u32 s75, s69, 0
	s_barrier
	v_readfirstlane_b32 s34, v84
	v_add_u32_e32 v84, 0x6000, v136
	v_readfirstlane_b32 s34, v84
	v_add_u32_e32 v84, 0xd000, v135
	v_readfirstlane_b32 s34, v84
	v_add_u32_e32 v84, 0xf000, v135
	v_readfirstlane_b32 s34, v84
	s_and_b64 vcc, exec, s[14:15]
	s_cbranch_vccnz .LBB4_145
	s_add_i32 s14, 0, 0x11000
	v_add_u32_e32 v1, s14, v1
	v_lshl_add_u64 v[82:83], v[122:123], 0, s[30:31]
	v_readfirstlane_b32 s14, v1
	s_mov_b32 m0, s14
	s_nop 0
	global_load_lds_dwordx4 v[82:83], off
.LBB4_145:
	s_waitcnt lgkmcnt(0)
	ds_read_b128 v[114:117], v90
	ds_read_b128 v[118:121], v90 offset:2048
	ds_read_b128 v[82:85], v146
	ds_read_b128 v[86:89], v146 offset:2048
	ds_read_b128 v[156:159], v146 offset:4096
	ds_read_b128 v[160:163], v146 offset:6144
	ds_read_b128 v[164:167], v146 offset:8192
	ds_read_b128 v[168:171], v146 offset:10240
	s_and_b64 vcc, exec, s[24:25]
	s_waitcnt lgkmcnt(5)
	v_mfma_f32_16x16x32_f16 v[18:21], v[114:117], v[82:85], v[18:21]
	s_mov_b32 m0, s82
	v_mfma_f32_16x16x32_f16 v[22:25], v[118:121], v[82:85], v[22:25]
	global_load_lds_dwordx4 v176, s[72:73]
	s_waitcnt lgkmcnt(4)
	v_mfma_f32_16x16x32_f16 v[26:29], v[114:117], v[86:89], v[26:29]
	s_mov_b32 m0, s83
	v_mfma_f32_16x16x32_f16 v[30:33], v[118:121], v[86:89], v[30:33]
	global_load_lds_dwordx4 v177, s[72:73]
	s_waitcnt lgkmcnt(2)
	v_mfma_f32_16x16x32_f16 v[42:45], v[114:117], v[160:163], v[42:45]
	s_mov_b32 m0, s84
	v_mfma_f32_16x16x32_f16 v[46:49], v[118:121], v[160:163], v[46:49]
	global_load_lds_dwordx4 v178, s[72:73]
	v_mfma_f32_16x16x32_f16 v[34:37], v[114:117], v[156:159], v[34:37]
	s_mov_b32 m0, s85
	v_mfma_f32_16x16x32_f16 v[38:41], v[118:121], v[156:159], v[38:41]
	global_load_lds_dwordx4 v179, s[72:73]
	ds_read_b128 v[156:159], v146 offset:12288
	ds_read_b128 v[160:163], v146 offset:14336
	s_waitcnt lgkmcnt(3)
	v_mfma_f32_16x16x32_f16 v[82:85], v[114:117], v[164:167], v[50:53]
	s_mov_b32 m0, s86
	v_mfma_f32_16x16x32_f16 v[86:89], v[118:121], v[164:167], v[54:57]
	global_load_lds_dwordx4 v180, s[74:75]
	s_nop 1
	s_waitcnt lgkmcnt(2)
	v_mfma_f32_16x16x32_f16 v[90:93], v[114:117], v[168:171], v[58:61]
	s_mov_b32 m0, s87
	v_mfma_f32_16x16x32_f16 v[94:97], v[118:121], v[168:171], v[62:65]
	global_load_lds_dwordx4 v181, s[74:75]
	s_waitcnt lgkmcnt(1)
	v_mfma_f32_16x16x32_f16 v[98:101], v[114:117], v[156:159], v[66:69]
	v_mfma_f32_16x16x32_f16 v[102:105], v[118:121], v[156:159], v[70:73]
	s_waitcnt lgkmcnt(0)
	v_mfma_f32_16x16x32_f16 v[106:109], v[114:117], v[160:163], v[74:77]
	v_mfma_f32_16x16x32_f16 v[110:113], v[118:121], v[160:163], v[78:81]
	s_cbranch_vccnz .LBB4_147
	ds_read_b128 v[50:53], v146 offset:16384
	s_waitcnt lgkmcnt(0)
	v_mfma_f32_16x16x32_f16 v[6:9], v[114:117], v[50:53], v[6:9]
	v_mfma_f32_16x16x32_f16 v[2:5], v[118:121], v[50:53], v[2:5]
